# attention softmax: exp arguments via in-place v_pk_fma_f32 (16 instead of 32 v_fmamk), bf16 pack reads swapped pairs directly (16 v_pk_mov removed); plus conv nt loads/remap/stagger
# speedup vs baseline: 1.0065x; 1.0065x over previous
; #define LAS __attribute__((address_space(3)))
;     ...
; #pragma unroll
;         for (int it = 0; it < 4; ++it) { const int id = F.tid + 512 * it, row = id >> 3, c8 = id & 7; *(LAS u32x4*)(Ks + row * KS_PITCH + c8 * 16) = kr[it]; }
; #pragma unroll
;         for (int it = 0; it < 2; ++it) { const int id = F.tid + 512 * it, rp = id >> 3, c8 = id & 7;
;             const unsigned a[4] = {va[it].x, va[it].y, va[it].z, va[it].w}, bq[4] = {vb[it].x, vb[it].y, vb[it].z, vb[it].w};
;             LAS unsigned char* vp = Vt + (c8 * 8) * VT_PITCH + rp * 4;
; #pragma unroll
;             for (int q = 0; q < 4; ++q) { *(LAS unsigned*)(vp + (2 * q) * VT_PITCH) = (a[q] & 0xffffu) | (bq[q] << 16); *(LAS unsigned*)(vp + (2 * q + 1) * VT_PITCH) = (a[q] >> 16) | (bq[q] & 0xffff0000u); } }
;         if (F.tid <= 128) LUT[1 + F.tid] = lutv;
;         if (F.tid == 129) LUT[0] = -1e30f;
;         __syncthreads();
;         const float bfar = LUT[129];
;     ...
;             constexpr float L2E = 1.4426950408889634f;
.LBB0_2219:
	s_waitcnt vmcnt(7)
	s_waitcnt vmcnt(6)
	s_waitcnt vmcnt(5)
	s_waitcnt vmcnt(4)
	s_waitcnt vmcnt(0)
	ds_write_b128 v218, v[16:19]
	ds_write_b128 v219, v[20:23]
	ds_write_b128 v220, v[24:27]
	ds_write_b128 v221, v[28:31]
	v_and_b32_e32 v16, 0xffff, v8
	v_lshrrev_b32_e32 v8, 16, v8
	s_mov_b32 s2, 0xffff0000
	v_lshl_or_b32 v16, v12, 16, v16
	v_and_or_b32 v8, v12, s2, v8
	v_add_u32_e32 v12, 0x9000, v222
	ds_write2_b32 v12, v16, v8 offset1:130
	v_and_b32_e32 v8, 0xffff, v9
	v_lshrrev_b32_e32 v9, 16, v9
	v_lshl_or_b32 v8, v13, 16, v8
	v_and_or_b32 v9, v13, s2, v9
	v_add_u32_e32 v12, 0x9400, v222
	ds_write2_b32 v12, v8, v9 offset0:4 offset1:134
	v_and_b32_e32 v8, 0xffff, v10
	v_lshrrev_b32_e32 v9, 16, v10
	v_lshl_or_b32 v8, v14, 16, v8
	v_and_or_b32 v9, v14, s2, v9
	v_add_u32_e32 v10, 0x9800, v222
	ds_write2_b32 v10, v8, v9 offset0:8 offset1:138
	v_and_b32_e32 v8, 0xffff, v11
	v_lshrrev_b32_e32 v9, 16, v11
	v_lshl_or_b32 v8, v15, 16, v8
	v_and_or_b32 v9, v15, s2, v9
	v_add_u32_e32 v10, 0x9c00, v222
	ds_write2_b32 v10, v8, v9 offset0:12 offset1:142
	v_and_b32_e32 v8, 0xffff, v0
	v_lshrrev_b32_e32 v0, 16, v0
	v_lshl_or_b32 v8, v4, 16, v8
	v_and_or_b32 v0, v4, s2, v0
	v_add_u32_e32 v4, 0x9000, v223
	ds_write2_b32 v4, v8, v0 offset1:130
	v_and_b32_e32 v0, 0xffff, v1
	v_lshrrev_b32_e32 v1, 16, v1
	v_lshl_or_b32 v0, v5, 16, v0
	v_and_or_b32 v1, v5, s2, v1
	v_add_u32_e32 v4, 0x9400, v223
	ds_write2_b32 v4, v0, v1 offset0:4 offset1:134
	v_and_b32_e32 v0, 0xffff, v2
	v_lshrrev_b32_e32 v1, 16, v2
	v_lshl_or_b32 v0, v6, 16, v0
	v_and_or_b32 v1, v6, s2, v1
	v_add_u32_e32 v2, 0x9800, v223
	ds_write2_b32 v2, v0, v1 offset0:8 offset1:138
	v_and_b32_e32 v0, 0xffff, v3
	v_lshrrev_b32_e32 v1, 16, v3
	v_lshl_or_b32 v0, v7, 16, v0
	v_and_or_b32 v1, v7, s2, v1
	v_add_u32_e32 v2, 0x9c00, v223
	ds_write2_b32 v2, v0, v1 offset0:12 offset1:142
	s_and_saveexec_b64 s[2:3], s[14:15]
	ds_write_b32 v213, v33 offset:4
	s_or_b64 exec, exec, s[2:3]
	s_and_saveexec_b64 s[2:3], s[16:17]
	v_mov_b32_e32 v0, s33
	v_mov_b32_e32 v1, 0xf149f2ca
	ds_write_b32 v0, v1
	s_or_b64 exec, exec, s[2:3]
	s_andn2_b64 vcc, exec, s[0:1]
	s_waitcnt lgkmcnt(0)
	s_barrier
	s_cbranch_vccnz .LBB0_2241
	v_mov_b32_e32 v0, s74
	ds_read_b32 v114, v0
	s_lshl_b32 s0, s4, 1
	s_mov_b32 s1, s45
	v_lshl_add_u64 v[116:117], v[144:145], 0, s[0:1]
	s_add_u32 s0, s69, s0
	s_addc_u32 s1, s89, 0
	s_lshl_b32 s2, s81, 3
	s_add_u32 s2, s70, s2
	v_mov_b64_e32 v[94:95], v[98:99]
	v_mov_b64_e32 v[90:91], v[102:103]
	v_mov_b64_e32 v[86:87], v[106:107]
	v_mov_b64_e32 v[82:83], v[110:111]
	s_addc_u32 s3, s71, 0
	s_waitcnt lgkmcnt(0)
	v_mov_b32_e32 v115, v114
	s_mov_b32 s19, s68
	v_mov_b64_e32 v[96:97], v[100:101]
	v_mov_b64_e32 v[92:93], v[104:105]
	v_mov_b64_e32 v[88:89], v[108:109]
	v_mov_b64_e32 v[84:85], v[112:113]
	v_mov_b32_e32 v228, 0x3fb8aa3b
	s_mov_b32 s23, 0xf149f2ca
	s_branch .LBB0_2226

; #define LAS __attribute__((address_space(3)))
; DI unsigned pk2(float lo, float hi) { f32x2 v = {lo, hi}; return __builtin_bit_cast(unsigned, __builtin_convertvector(v, bf16v2)); }
;     ...
;                 const float nm = -mnew * L2E;
; #pragma unroll
;                 for (int k2 = 0; k2 < 2; ++k2) { const int kt = 2 * ck + k2;
; #pragma unroll
;                     for (int i = 0; i < 16; i += 4) { const float p0 = __builtin_amdgcn_exp2f(__builtin_fmaf(sacc[k2][i], L2E, nm)), p1 = __builtin_amdgcn_exp2f(__builtin_fmaf(sacc[k2][i + 1], L2E, nm)),
;                                                                   p2 = __builtin_amdgcn_exp2f(__builtin_fmaf(sacc[k2][i + 2], L2E, nm)), p3 = __builtin_amdgcn_exp2f(__builtin_fmaf(sacc[k2][i + 3], L2E, nm));
;                         sacc[k2][i] = p0; sacc[k2][i + 1] = p1; sacc[k2][i + 2] = p2; sacc[k2][i + 3] = p3; ls0 += p0; ls1 += p1; ls2 += p2; ls3 += p3; }
; #pragma unroll
;                     for (int cc = 0; cc < 2; ++cc) {
;                         u32x4 pw; pw.x = pk2(sacc[k2][8 * cc], sacc[k2][8 * cc + 1]); pw.y = pk2(sacc[k2][8 * cc + 2], sacc[k2][8 * cc + 3]); pw.z = pk2(sacc[k2][8 * cc + 4], sacc[k2][8 * cc + 5]); pw.w = pk2(sacc[k2][8 * cc + 6], sacc[k2][8 * cc + 7]);
;                         const bf16x8 pf = __builtin_bit_cast(bf16x8, pw);
;                         const int key0 = 32 * kt + 16 * cc + 4 * half;
; #pragma unroll
;                         for (int dt = 0; dt < 2; ++dt) { const LAS unsigned char* vb = Vt + (32 * dt + qi) * VT_PITCH + key0 * 2;
;                             const u32x2 va = *(const LAS u32x2*)vb, vb2 = *(const LAS u32x2*)(vb + 16);
;                             u32x4 vw; vw.x = va.x; vw.y = va.y; vw.z = vb2.x; vw.w = vb2.y;
;                             oacc[dt] = __builtin_amdgcn_mfma_f32_32x32x16_bf16(__builtin_bit_cast(bf16x8, vw), pf, oacc[dt], 0, 0, 0); } } }
.LBB0_2235:
	v_mul_f32_e32 v33, 0xbfb8aa3b, v32
	v_pk_fma_f32 v[126:127], v[126:127], v[228:229], v[32:33] op_sel:[0,0,1] op_sel_hi:[1,0,1]
	v_pk_fma_f32 v[122:123], v[122:123], v[228:229], v[32:33] op_sel:[0,0,1] op_sel_hi:[1,0,1]
	v_exp_f32_e32 v63, v126
	v_pk_fma_f32 v[128:129], v[128:129], v[228:229], v[32:33] op_sel:[0,0,1] op_sel_hi:[1,0,1]
	v_exp_f32_e32 v62, v127
	v_pk_fma_f32 v[124:125], v[124:125], v[228:229], v[32:33] op_sel:[0,0,1] op_sel_hi:[1,0,1]
	v_exp_f32_e32 v61, v122
	v_exp_f32_e32 v60, v123
	v_exp_f32_e32 v123, v128
	v_exp_f32_e32 v122, v129
	v_pk_fma_f32 v[130:131], v[130:131], v[228:229], v[32:33] op_sel:[0,0,1] op_sel_hi:[1,0,1]
	v_exp_f32_e32 v35, v124
	v_exp_f32_e32 v34, v125
	v_exp_f32_e32 v125, v130
	v_exp_f32_e32 v124, v131
	v_pk_fma_f32 v[132:133], v[132:133], v[228:229], v[32:33] op_sel:[0,0,1] op_sel_hi:[1,0,1]
	v_pk_fma_f32 v[164:165], v[164:165], v[228:229], v[32:33] op_sel:[0,0,1] op_sel_hi:[1,0,1]
	v_exp_f32_e32 v127, v132
	v_exp_f32_e32 v126, v133
	v_exp_f32_e32 v133, v164
	v_exp_f32_e32 v132, v165
	v_pk_fma_f32 v[134:135], v[134:135], v[228:229], v[32:33] op_sel:[0,0,1] op_sel_hi:[1,0,1]
	v_pk_fma_f32 v[166:167], v[166:167], v[228:229], v[32:33] op_sel:[0,0,1] op_sel_hi:[1,0,1]
	v_exp_f32_e32 v129, v134
	v_exp_f32_e32 v128, v135
	v_exp_f32_e32 v135, v166
	v_exp_f32_e32 v134, v167
	v_pk_fma_f32 v[136:137], v[136:137], v[228:229], v[32:33] op_sel:[0,0,1] op_sel_hi:[1,0,1]
	v_pk_fma_f32 v[168:169], v[168:169], v[228:229], v[32:33] op_sel:[0,0,1] op_sel_hi:[1,0,1]
	v_exp_f32_e32 v131, v136
	v_exp_f32_e32 v130, v137
	v_exp_f32_e32 v137, v168
	v_exp_f32_e32 v136, v169
	v_pk_fma_f32 v[170:171], v[170:171], v[228:229], v[32:33] op_sel:[0,0,1] op_sel_hi:[1,0,1]
	v_pk_fma_f32 v[172:173], v[172:173], v[228:229], v[32:33] op_sel:[0,0,1] op_sel_hi:[1,0,1]
	v_exp_f32_e32 v165, v170
	v_exp_f32_e32 v164, v171
	v_add_u32_e32 v58, 0x4000, v216
	v_exp_f32_e32 v167, v172
	v_exp_f32_e32 v166, v173
	v_pk_fma_f32 v[174:175], v[174:175], v[228:229], v[32:33] op_sel:[0,0,1] op_sel_hi:[1,0,1]
	ds_read2_b64 v[36:39], v216 offset1:2
	ds_read2_b64 v[40:43], v216 offset0:4 offset1:6
	ds_read2_b64 v[44:47], v58 offset0:32 offset1:34
	ds_read2_b64 v[48:51], v58 offset0:36 offset1:38
	v_pk_fma_f32 v[138:139], v[138:139], v[228:229], v[32:33] op_sel:[0,0,1] op_sel_hi:[1,0,1]
	v_exp_f32_e32 v169, v174
	v_exp_f32_e32 v168, v175
	v_cvt_pk_bf16_f32 v52, v61, v60
	v_cvt_pk_bf16_f32 v53, v35, v34
	v_cvt_pk_bf16_f32 v54, v63, v62
	v_cvt_pk_bf16_f32 v55, v123, v122
	v_exp_f32_e32 v171, v138
	v_exp_f32_e32 v170, v139
	s_waitcnt lgkmcnt(3)
	v_mfma_f32_32x32x16_bf16 v[16:31], v[36:39], v[52:55], v[16:31]
	v_pk_fma_f32 v[140:141], v[140:141], v[228:229], v[32:33] op_sel:[0,0,1] op_sel_hi:[1,0,1]
	v_cvt_pk_bf16_f32 v36, v125, v124
	v_exp_f32_e32 v139, v140
	s_waitcnt lgkmcnt(1)
	v_mfma_f32_32x32x16_bf16 v[0:15], v[44:47], v[52:55], v[0:15]
	v_cvt_pk_bf16_f32 v38, v129, v128
	v_cvt_pk_bf16_f32 v37, v127, v126
	v_pk_add_f32 v[60:61], v[60:61], v[120:121]
	v_cvt_pk_bf16_f32 v39, v131, v130
	v_exp_f32_e32 v138, v141
	s_nop 0
	v_mfma_f32_32x32x16_bf16 v[16:31], v[40:43], v[36:39], v[16:31]
	ds_read2_b64 v[40:43], v216 offset0:8 offset1:10
	ds_read2_b64 v[44:47], v58 offset0:40 offset1:42
	ds_read2_b64 v[52:55], v216 offset0:12 offset1:14
	ds_read2_b64 v[56:59], v58 offset0:44 offset1:46
	v_add_f32_e64 v34, v34, v118
	v_add_f32_e64 v35, v35, v119
	v_pk_add_f32 v[34:35], v[122:123], v[34:35]
	s_sub_i32 s21, s21, 64
	v_pk_add_f32 v[34:35], v[126:127], v[34:35]
	s_add_i32 s22, s22, 64
	s_waitcnt lgkmcnt(4)
	v_mfma_f32_32x32x16_bf16 v[0:15], v[48:51], v[36:39], v[0:15]
	v_cvt_pk_bf16_f32 v37, v135, v134
	v_cvt_pk_bf16_f32 v36, v133, v132
	v_cvt_pk_bf16_f32 v38, v137, v136
	v_cvt_pk_bf16_f32 v39, v165, v164
	v_pk_add_f32 v[34:35], v[130:131], v[34:35]
	s_cmpk_eq_i32 s21, 0xff00
	s_waitcnt lgkmcnt(3)
	v_mfma_f32_32x32x16_bf16 v[16:31], v[40:43], v[36:39], v[16:31]
	v_add_f32_e64 v40, v62, v60
	v_add_f32_e64 v41, v63, v61
	v_pk_add_f32 v[40:41], v[124:125], v[40:41]
	v_pk_add_f32 v[34:35], v[134:135], v[34:35]
	v_pk_add_f32 v[40:41], v[128:129], v[40:41]
	v_pk_add_f32 v[34:35], v[164:165], v[34:35]
	v_pk_add_f32 v[40:41], v[132:133], v[40:41]
	s_waitcnt lgkmcnt(2)
	v_mfma_f32_32x32x16_bf16 v[0:15], v[44:47], v[36:39], v[0:15]
	v_cvt_pk_bf16_f32 v36, v167, v166
	v_pk_add_f32 v[40:41], v[136:137], v[40:41]
	v_cvt_pk_bf16_f32 v37, v169, v168
	v_pk_add_f32 v[40:41], v[166:167], v[40:41]
	v_cvt_pk_bf16_f32 v38, v171, v170
	v_cvt_pk_bf16_f32 v39, v139, v138
	v_pk_add_f32 v[34:35], v[168:169], v[34:35]
	v_pk_add_f32 v[120:121], v[170:171], v[40:41]
	s_waitcnt lgkmcnt(1)
	v_mfma_f32_32x32x16_bf16 v[16:31], v[52:55], v[36:39], v[16:31]
	v_add_f32_e64 v118, v138, v34
	v_add_f32_e64 v119, v139, v35
	v_add_u32_e32 v216, 0x80, v216
	v_add_u32_e32 v251, 0x2400, v251
	s_cselect_b64 s[6:7], -1, 0
	s_waitcnt lgkmcnt(0)
	v_mfma_f32_32x32x16_bf16 v[0:15], v[56:59], v[36:39], v[0:15]
	s_and_b64 vcc, exec, s[6:7]
	s_cbranch_vccnz .LBB0_2238
